# h1 barrier placed in the middle of the second own k-step so the next B-fragment reads are covered by 8 MFMAs
# speedup vs baseline: 1.0178x; 1.0022x over previous
.LBB1_4:
	s_and_saveexec_b64 s[8:9], s[2:3]
	v_perm_b32 v5, v1, v102, s23
	v_perm_b32 v9, v121, v103, s23
	v_perm_b32 v17, v144, v115, s23
	v_perm_b32 v29, v145, v116, s23
	s_or_b64 exec, exec, s[8:9]
	v_mfma_f32_16x16x32_f16 v[164:167], v[30:33], v[2:5], 0
	v_mfma_f32_16x16x32_f16 v[180:183], v[22:25], v[2:5], 0
	s_cmp_lg_u32 s22, 0x818000
	v_mfma_f32_16x16x32_f16 v[168:171], v[30:33], v[6:9], 0
	v_mfma_f32_16x16x32_f16 v[184:187], v[22:25], v[6:9], 0
	s_cselect_b32 s9, s11, 15
	v_mfma_f32_16x16x32_f16 v[172:175], v[30:33], v[14:17], 0
	v_mfma_f32_16x16x32_f16 v[188:191], v[22:25], v[14:17], 0
	v_mfma_f32_16x16x32_f16 v[176:179], v[30:33], v[26:29], 0
	v_mfma_f32_16x16x32_f16 v[192:195], v[22:25], v[26:29], 0
	v_mfma_f32_16x16x32_f16 v[196:199], v[18:21], v[2:5], 0
	v_cvt_pk_f16_f32 v122, v164, v165
	v_cvt_pk_f16_f32 v123, v166, v167
	v_pk_max_f16 v122, v122, 0
	v_pk_max_f16 v123, v123, 0
	v_cvt_pk_f16_f32 v124, v180, v181
	v_cvt_pk_f16_f32 v125, v182, v183
	v_pk_max_f16 v124, v124, 0
	v_pk_max_f16 v125, v125, 0
	ds_write_b128 v107, v[122:125]
	v_mfma_f32_16x16x32_f16 v[212:215], v[10:13], v[2:5], 0
	v_cvt_pk_f16_f32 v126, v168, v169
	v_cvt_pk_f16_f32 v127, v170, v171
	v_pk_max_f16 v126, v126, 0
	v_pk_max_f16 v127, v127, 0
	v_cvt_pk_f16_f32 v128, v184, v185
	v_cvt_pk_f16_f32 v129, v186, v187
	v_pk_max_f16 v128, v128, 0
	v_pk_max_f16 v129, v129, 0
	ds_write_b128 v107, v[126:129] offset:16384
	v_mfma_f32_16x16x32_f16 v[200:203], v[18:21], v[6:9], 0
	v_cvt_pk_f16_f32 v134, v172, v173
	v_cvt_pk_f16_f32 v135, v174, v175
	v_pk_max_f16 v134, v134, 0
	v_pk_max_f16 v135, v135, 0
	v_cvt_pk_f16_f32 v136, v188, v189
	v_cvt_pk_f16_f32 v137, v190, v191
	v_pk_max_f16 v136, v136, 0
	v_pk_max_f16 v137, v137, 0
	ds_write_b128 v107, v[134:137] offset:32768
	v_mfma_f32_16x16x32_f16 v[216:219], v[10:13], v[6:9], 0
	v_cvt_pk_f16_f32 v138, v176, v177
	v_cvt_pk_f16_f32 v139, v178, v179
	v_pk_max_f16 v138, v138, 0
	v_pk_max_f16 v139, v139, 0
	v_cvt_pk_f16_f32 v140, v192, v193
	v_cvt_pk_f16_f32 v141, v194, v195
	v_pk_max_f16 v140, v140, 0
	v_pk_max_f16 v141, v141, 0
	ds_write_b128 v107, v[138:141] offset:49152
	v_mfma_f32_16x16x32_f16 v[204:207], v[18:21], v[14:17], 0
	v_cvt_pk_f16_f32 v142, v196, v197
	v_cvt_pk_f16_f32 v143, v198, v199
	v_pk_max_f16 v142, v142, 0
	v_pk_max_f16 v143, v143, 0
	v_cvt_pk_f16_f32 v144, v212, v213
	v_cvt_pk_f16_f32 v145, v214, v215
	v_pk_max_f16 v144, v144, 0
	v_pk_max_f16 v145, v145, 0
	ds_write_b128 v108, v[142:145]
	v_mfma_f32_16x16x32_f16 v[220:223], v[10:13], v[14:17], 0
	v_cvt_pk_f16_f32 v152, v200, v201
	v_cvt_pk_f16_f32 v153, v202, v203
	v_pk_max_f16 v152, v152, 0
	v_pk_max_f16 v153, v153, 0
	v_cvt_pk_f16_f32 v154, v216, v217
	v_cvt_pk_f16_f32 v155, v218, v219
	v_pk_max_f16 v154, v154, 0
	v_pk_max_f16 v155, v155, 0
	ds_write_b128 v108, v[152:155] offset:16384
	v_mfma_f32_16x16x32_f16 v[208:211], v[18:21], v[26:29], 0
	v_mfma_f32_16x16x32_f16 v[224:227], v[10:13], v[26:29], 0
	v_cvt_pk_f16_f32 v156, v204, v205
	v_cvt_pk_f16_f32 v157, v206, v207
	v_pk_max_f16 v156, v156, 0
	v_pk_max_f16 v157, v157, 0
	v_cvt_pk_f16_f32 v158, v220, v221
	v_cvt_pk_f16_f32 v159, v222, v223
	v_pk_max_f16 v158, v158, 0
	v_pk_max_f16 v159, v159, 0
	ds_write_b128 v108, v[156:159] offset:32768
	v_cvt_pk_f16_f32 v160, v208, v209
	v_cvt_pk_f16_f32 v161, v210, v211
	v_pk_max_f16 v160, v160, 0
	v_pk_max_f16 v161, v161, 0
	v_cvt_pk_f16_f32 v162, v224, v225
	v_cvt_pk_f16_f32 v163, v226, v227
	v_pk_max_f16 v162, v162, 0
	v_pk_max_f16 v163, v163, 0
	ds_write_b128 v108, v[160:163] offset:49152
	v_add_u32_e32 v111, s64, v111
	v_add_u32_e32 v98, s65, v98
	s_lshl_b32 s20, s9, 7
	v_lshl_add_u64 v[0:1], s[20:21], 3, v[132:133]
	s_add_i32 s25, s22, s34
	s_lshl_b32 s8, s9, 8
	buffer_load_dwordx4 v[192:195], v147, s[16:19], s25 offen
	buffer_load_dwordx4 v[196:199], v148, s[16:19], s25 offen
	buffer_load_dwordx4 v[200:203], v149, s[16:19], s25 offen
	buffer_load_dwordx4 v[204:207], v150, s[16:19], s25 offen
	s_waitcnt vmcnt(19)
	v_mfma_f32_16x16x32_f16 v[164:167], v[58:61], v[122:125], v[240:243]
	v_mfma_f32_16x16x32_f16 v[168:171], v[58:61], v[126:129], v[240:243]
	v_mfma_f32_16x16x32_f16 v[172:175], v[58:61], v[134:137], v[240:243]
	v_mfma_f32_16x16x32_f16 v[10:13], v[58:61], v[138:141], v[240:243]
	s_waitcnt vmcnt(18)
	v_mfma_f32_16x16x32_f16 v[58:61], v[54:57], v[122:125], v[244:247]
	v_mfma_f32_16x16x32_f16 v[176:179], v[54:57], v[126:129], v[244:247]
	v_mfma_f32_16x16x32_f16 v[180:183], v[54:57], v[134:137], v[244:247]
	v_mfma_f32_16x16x32_f16 v[18:21], v[54:57], v[138:141], v[244:247]
	s_waitcnt vmcnt(17)
	v_mfma_f32_16x16x32_f16 v[54:57], v[50:53], v[122:125], v[248:251]
	v_mfma_f32_16x16x32_f16 v[184:187], v[50:53], v[126:129], v[248:251]
	v_mfma_f32_16x16x32_f16 v[188:191], v[50:53], v[134:137], v[248:251]
	v_mfma_f32_16x16x32_f16 v[22:25], v[50:53], v[138:141], v[248:251]
	s_waitcnt vmcnt(16)
	v_mfma_f32_16x16x32_f16 v[50:53], v[38:41], v[122:125], v[252:255]
	v_mfma_f32_16x16x32_f16 v[122:125], v[38:41], v[126:129], v[252:255]
	v_mfma_f32_16x16x32_f16 v[126:129], v[38:41], v[134:137], v[252:255]
	v_mfma_f32_16x16x32_f16 v[38:41], v[38:41], v[138:141], v[252:255]
	s_add_i32 s9, s22, s35
	s_waitcnt vmcnt(15)
	v_mfma_f32_16x16x32_f16 v[164:167], v[94:97], v[142:145], v[164:167]
	v_mfma_f32_16x16x32_f16 v[168:171], v[94:97], v[152:155], v[168:171]
	s_waitcnt vmcnt(14)
	v_mfma_f32_16x16x32_f16 v[58:61], v[90:93], v[142:145], v[58:61]
	v_mfma_f32_16x16x32_f16 v[176:179], v[90:93], v[152:155], v[176:179]
	s_waitcnt vmcnt(13)
	v_mfma_f32_16x16x32_f16 v[54:57], v[78:81], v[142:145], v[54:57]
	v_mfma_f32_16x16x32_f16 v[184:187], v[78:81], v[152:155], v[184:187]
	s_waitcnt vmcnt(12)
	v_mfma_f32_16x16x32_f16 v[50:53], v[34:37], v[142:145], v[50:53]
	buffer_load_dwordx4 v[140:143], v147, s[16:19], s9 offen
	buffer_load_dwordx4 v[220:223], v148, s[16:19], s9 offen
	v_mfma_f32_16x16x32_f16 v[122:125], v[34:37], v[152:155], v[122:125]
	buffer_load_dwordx4 v[152:155], v149, s[16:19], s9 offen
	buffer_load_dwordx4 v[224:227], v150, s[16:19], s9 offen
	s_mov_b32 s9, s21
	s_waitcnt lgkmcnt(0)
	s_barrier
	v_add_u32_e32 v99, s66, v99
	ds_read_b128 v[136:139], v99
	ds_read_b128 v[208:211], v99 offset:16384
	ds_read_b128 v[212:215], v99 offset:32768
	ds_read_b128 v[216:219], v99 offset:49152
	v_mfma_f32_16x16x32_f16 v[172:175], v[94:97], v[156:159], v[172:175]
	v_mfma_f32_16x16x32_f16 v[94:97], v[94:97], v[160:163], v[10:13]
	s_nop 2
	v_lshl_add_u64 v[10:11], s[8:9], 4, v[130:131]
	v_mfma_f32_16x16x32_f16 v[180:183], v[90:93], v[156:159], v[180:183]
	v_mfma_f32_16x16x32_f16 v[90:93], v[90:93], v[160:163], v[18:21]
	v_mfma_f32_16x16x32_f16 v[188:191], v[78:81], v[156:159], v[188:191]
	v_mfma_f32_16x16x32_f16 v[78:81], v[78:81], v[160:163], v[22:25]
	global_load_dwordx4 v[30:33], v[10:11], off
	s_nop 1
	global_load_dwordx4 v[22:25], v[10:11], off offset:1024
	global_load_dwordx4 v[18:21], v[10:11], off offset:2048
	s_nop 0
	global_load_dwordx4 v[10:13], v[10:11], off offset:3072
	s_nop 0
	global_load_dwordx2 v[134:135], v[0:1], off
	v_mfma_f32_16x16x32_f16 v[126:129], v[34:37], v[156:159], v[126:129]
	v_mfma_f32_16x16x32_f16 v[34:37], v[34:37], v[160:163], v[38:41]
	s_nop 2
	v_add_u32_e32 v100, s67, v100
	ds_read_b128 v[38:41], v100
	ds_read_b128 v[156:159], v100 offset:16384
	ds_read_b128 v[160:163], v100 offset:32768
	ds_read_b128 v[228:231], v100 offset:49152
	s_add_i32 s8, s22, s36
	s_waitcnt vmcnt(20) lgkmcnt(7)
	v_mfma_f32_16x16x32_f16 v[164:167], v[82:85], v[136:139], v[164:167]
	s_waitcnt lgkmcnt(6)
	v_mfma_f32_16x16x32_f16 v[168:171], v[82:85], v[208:211], v[168:171]
	s_waitcnt lgkmcnt(5)
	v_mfma_f32_16x16x32_f16 v[172:175], v[82:85], v[212:215], v[172:175]
	s_waitcnt lgkmcnt(4)
	v_mfma_f32_16x16x32_f16 v[82:85], v[82:85], v[216:219], v[94:97]
	s_waitcnt vmcnt(19)
	v_mfma_f32_16x16x32_f16 v[58:61], v[70:73], v[136:139], v[58:61]
	v_mfma_f32_16x16x32_f16 v[94:97], v[70:73], v[208:211], v[176:179]
	v_mfma_f32_16x16x32_f16 v[176:179], v[70:73], v[212:215], v[180:183]
	v_mfma_f32_16x16x32_f16 v[70:73], v[70:73], v[216:219], v[90:93]
	s_waitcnt vmcnt(18)
	v_mfma_f32_16x16x32_f16 v[54:57], v[62:65], v[136:139], v[54:57]
	v_mfma_f32_16x16x32_f16 v[90:93], v[62:65], v[208:211], v[184:187]
	v_mfma_f32_16x16x32_f16 v[180:183], v[62:65], v[212:215], v[188:191]
	v_mfma_f32_16x16x32_f16 v[62:65], v[62:65], v[216:219], v[78:81]
	s_waitcnt vmcnt(17)
	v_mfma_f32_16x16x32_f16 v[50:53], v[42:45], v[136:139], v[50:53]
	v_mfma_f32_16x16x32_f16 v[78:81], v[42:45], v[208:211], v[122:125]
	v_mfma_f32_16x16x32_f16 v[122:125], v[42:45], v[212:215], v[126:129]
	s_nop 2
	buffer_load_dwordx4 v[126:129], v147, s[16:19], s8 offen
	buffer_load_dwordx4 v[136:139], v148, s[16:19], s8 offen
	buffer_load_dwordx4 v[184:187], v149, s[16:19], s8 offen
	buffer_load_dwordx4 v[188:191], v150, s[16:19], s8 offen
	v_mfma_f32_16x16x32_f16 v[34:37], v[42:45], v[216:219], v[34:37]
	v_add_u32_e32 v111, s68, v111
	ds_read_b128 v[42:45], v111
	ds_read_b128 v[208:211], v111 offset:16384
	ds_read_b128 v[212:215], v111 offset:32768
	ds_read_b128 v[216:219], v111 offset:49152
	s_add_i32 s8, s22, s37
	s_waitcnt vmcnt(20) lgkmcnt(7)
	v_mfma_f32_16x16x32_f16 v[164:167], v[86:89], v[38:41], v[164:167]
	s_waitcnt lgkmcnt(6)
	v_mfma_f32_16x16x32_f16 v[168:171], v[86:89], v[156:159], v[168:171]
	s_waitcnt lgkmcnt(5)
	v_mfma_f32_16x16x32_f16 v[172:175], v[86:89], v[160:163], v[172:175]
	s_waitcnt lgkmcnt(4)
	v_mfma_f32_16x16x32_f16 v[82:85], v[86:89], v[228:231], v[82:85]
	s_waitcnt vmcnt(19)
	v_mfma_f32_16x16x32_f16 v[58:61], v[74:77], v[38:41], v[58:61]
	v_mfma_f32_16x16x32_f16 v[86:89], v[74:77], v[156:159], v[94:97]
	v_mfma_f32_16x16x32_f16 v[94:97], v[74:77], v[160:163], v[176:179]
	v_mfma_f32_16x16x32_f16 v[70:73], v[74:77], v[228:231], v[70:73]
	s_waitcnt vmcnt(18)
	v_mfma_f32_16x16x32_f16 v[54:57], v[66:69], v[38:41], v[54:57]
	v_mfma_f32_16x16x32_f16 v[74:77], v[66:69], v[156:159], v[90:93]
	v_mfma_f32_16x16x32_f16 v[90:93], v[66:69], v[160:163], v[180:183]
	v_mfma_f32_16x16x32_f16 v[62:65], v[66:69], v[228:231], v[62:65]
	s_waitcnt vmcnt(17)
	v_mfma_f32_16x16x32_f16 v[38:41], v[46:49], v[38:41], v[50:53]
	v_mfma_f32_16x16x32_f16 v[50:53], v[46:49], v[156:159], v[78:81]
	v_mfma_f32_16x16x32_f16 v[66:69], v[46:49], v[160:163], v[122:125]
	s_nop 1
	buffer_load_dwordx4 v[78:81], v147, s[16:19], s8 offen
	buffer_load_dwordx4 v[122:125], v148, s[16:19], s8 offen
	buffer_load_dwordx4 v[156:159], v149, s[16:19], s8 offen
	buffer_load_dwordx4 v[160:163], v150, s[16:19], s8 offen
	v_mfma_f32_16x16x32_f16 v[34:37], v[46:49], v[228:231], v[34:37]
	v_add_u32_e32 v98, s69, v98
	ds_read_b128 v[46:49], v98
	ds_read_b128 v[176:179], v98 offset:16384
	ds_read_b128 v[180:183], v98 offset:32768
	ds_read_b128 v[228:231], v98 offset:49152
	s_add_i32 s8, s22, s38
	s_waitcnt vmcnt(20) lgkmcnt(7)
	v_mfma_f32_16x16x32_f16 v[164:167], v[192:195], v[42:45], v[164:167]
	s_waitcnt lgkmcnt(6)
	v_mfma_f32_16x16x32_f16 v[168:171], v[192:195], v[208:211], v[168:171]
	s_waitcnt lgkmcnt(5)
	v_mfma_f32_16x16x32_f16 v[172:175], v[192:195], v[212:215], v[172:175]
	s_waitcnt lgkmcnt(4)
	v_mfma_f32_16x16x32_f16 v[82:85], v[192:195], v[216:219], v[82:85]
	s_waitcnt vmcnt(19)
	v_mfma_f32_16x16x32_f16 v[58:61], v[196:199], v[42:45], v[58:61]
	v_mfma_f32_16x16x32_f16 v[86:89], v[196:199], v[208:211], v[86:89]
	v_mfma_f32_16x16x32_f16 v[94:97], v[196:199], v[212:215], v[94:97]
	v_mfma_f32_16x16x32_f16 v[70:73], v[196:199], v[216:219], v[70:73]
	s_waitcnt vmcnt(18)
	v_mfma_f32_16x16x32_f16 v[54:57], v[200:203], v[42:45], v[54:57]
	v_mfma_f32_16x16x32_f16 v[74:77], v[200:203], v[208:211], v[74:77]
	v_mfma_f32_16x16x32_f16 v[90:93], v[200:203], v[212:215], v[90:93]
	v_mfma_f32_16x16x32_f16 v[62:65], v[200:203], v[216:219], v[62:65]
	s_waitcnt vmcnt(17)
	v_mfma_f32_16x16x32_f16 v[38:41], v[204:207], v[42:45], v[38:41]
	v_mfma_f32_16x16x32_f16 v[42:45], v[204:207], v[208:211], v[50:53]
	v_mfma_f32_16x16x32_f16 v[50:53], v[204:207], v[212:215], v[66:69]
	s_nop 2
	buffer_load_dwordx4 v[66:69], v147, s[16:19], s8 offen
	buffer_load_dwordx4 v[192:195], v148, s[16:19], s8 offen
	buffer_load_dwordx4 v[196:199], v149, s[16:19], s8 offen
	buffer_load_dwordx4 v[200:203], v150, s[16:19], s8 offen
	v_mfma_f32_16x16x32_f16 v[34:37], v[204:207], v[216:219], v[34:37]
	v_add_u32_e32 v99, s70, v99
	ds_read_b128 v[204:207], v99
	ds_read_b128 v[208:211], v99 offset:16384
	ds_read_b128 v[212:215], v99 offset:32768
	ds_read_b128 v[216:219], v99 offset:49152
	s_add_i32 s8, s22, s39
	s_waitcnt vmcnt(20) lgkmcnt(7)
	v_mfma_f32_16x16x32_f16 v[164:167], v[140:143], v[46:49], v[164:167]
	s_waitcnt lgkmcnt(6)
	v_mfma_f32_16x16x32_f16 v[168:171], v[140:143], v[176:179], v[168:171]
	s_waitcnt lgkmcnt(5)
	v_mfma_f32_16x16x32_f16 v[172:175], v[140:143], v[180:183], v[172:175]
	s_waitcnt lgkmcnt(4)
	v_mfma_f32_16x16x32_f16 v[82:85], v[140:143], v[228:231], v[82:85]
	s_waitcnt vmcnt(19)
	v_mfma_f32_16x16x32_f16 v[58:61], v[220:223], v[46:49], v[58:61]
	v_mfma_f32_16x16x32_f16 v[86:89], v[220:223], v[176:179], v[86:89]
	s_waitcnt vmcnt(18)
	v_mfma_f32_16x16x32_f16 v[54:57], v[152:155], v[46:49], v[54:57]
	v_mfma_f32_16x16x32_f16 v[74:77], v[152:155], v[176:179], v[74:77]
	v_mfma_f32_16x16x32_f16 v[90:93], v[152:155], v[180:183], v[90:93]
	v_mfma_f32_16x16x32_f16 v[62:65], v[152:155], v[228:231], v[62:65]
	s_waitcnt vmcnt(17)
	v_mfma_f32_16x16x32_f16 v[38:41], v[224:227], v[46:49], v[38:41]
	v_mfma_f32_16x16x32_f16 v[42:45], v[224:227], v[176:179], v[42:45]
	v_mfma_f32_16x16x32_f16 v[46:49], v[224:227], v[180:183], v[50:53]
	s_nop 2
	buffer_load_dwordx4 v[50:53], v147, s[16:19], s8 offen
	buffer_load_dwordx4 v[140:143], v148, s[16:19], s8 offen
	buffer_load_dwordx4 v[152:155], v149, s[16:19], s8 offen
	buffer_load_dwordx4 v[176:179], v150, s[16:19], s8 offen
	v_mfma_f32_16x16x32_f16 v[94:97], v[220:223], v[180:183], v[94:97]
	v_mfma_f32_16x16x32_f16 v[70:73], v[220:223], v[228:231], v[70:73]
	v_mfma_f32_16x16x32_f16 v[34:37], v[224:227], v[228:231], v[34:37]
	v_add_u32_e32 v100, s71, v100
	ds_read_b128 v[180:183], v100
	ds_read_b128 v[220:223], v100 offset:16384
	ds_read_b128 v[224:227], v100 offset:32768
	ds_read_b128 v[228:231], v100 offset:49152
	s_add_i32 s8, s22, s40
	s_waitcnt vmcnt(15) lgkmcnt(7)
	v_mfma_f32_16x16x32_f16 v[164:167], v[126:129], v[204:207], v[164:167]
	s_waitcnt lgkmcnt(6)
	v_mfma_f32_16x16x32_f16 v[168:171], v[126:129], v[208:211], v[168:171]
	s_waitcnt lgkmcnt(5)
	v_mfma_f32_16x16x32_f16 v[172:175], v[126:129], v[212:215], v[172:175]
	s_waitcnt lgkmcnt(4)
	v_mfma_f32_16x16x32_f16 v[82:85], v[126:129], v[216:219], v[82:85]
	s_waitcnt vmcnt(14)
	v_mfma_f32_16x16x32_f16 v[58:61], v[136:139], v[204:207], v[58:61]
	v_mfma_f32_16x16x32_f16 v[86:89], v[136:139], v[208:211], v[86:89]
	v_mfma_f32_16x16x32_f16 v[94:97], v[136:139], v[212:215], v[94:97]
	v_mfma_f32_16x16x32_f16 v[70:73], v[136:139], v[216:219], v[70:73]
	s_waitcnt vmcnt(13)
	v_mfma_f32_16x16x32_f16 v[54:57], v[184:187], v[204:207], v[54:57]
	v_mfma_f32_16x16x32_f16 v[74:77], v[184:187], v[208:211], v[74:77]
	v_mfma_f32_16x16x32_f16 v[90:93], v[184:187], v[212:215], v[90:93]
	v_mfma_f32_16x16x32_f16 v[62:65], v[184:187], v[216:219], v[62:65]
	s_waitcnt vmcnt(12)
	v_mfma_f32_16x16x32_f16 v[38:41], v[188:191], v[204:207], v[38:41]
	buffer_load_dwordx4 v[126:129], v147, s[16:19], s8 offen
	buffer_load_dwordx4 v[136:139], v148, s[16:19], s8 offen
	buffer_load_dwordx4 v[184:187], v149, s[16:19], s8 offen
	buffer_load_dwordx4 v[204:207], v150, s[16:19], s8 offen
	v_mfma_f32_16x16x32_f16 v[42:45], v[188:191], v[208:211], v[42:45]
	v_mfma_f32_16x16x32_f16 v[46:49], v[188:191], v[212:215], v[46:49]
	v_mfma_f32_16x16x32_f16 v[34:37], v[188:191], v[216:219], v[34:37]
	v_add_u32_e32 v111, s72, v111
	ds_read_b128 v[188:191], v111
	ds_read_b128 v[208:211], v111 offset:16384
	ds_read_b128 v[212:215], v111 offset:32768
	ds_read_b128 v[216:219], v111 offset:49152
	s_add_i32 s8, s22, s41
	s_waitcnt vmcnt(15) lgkmcnt(7)
	v_mfma_f32_16x16x32_f16 v[164:167], v[78:81], v[180:183], v[164:167]
	s_waitcnt lgkmcnt(6)
	v_mfma_f32_16x16x32_f16 v[168:171], v[78:81], v[220:223], v[168:171]
	s_waitcnt lgkmcnt(5)
	v_mfma_f32_16x16x32_f16 v[172:175], v[78:81], v[224:227], v[172:175]
	s_waitcnt lgkmcnt(4)
	v_mfma_f32_16x16x32_f16 v[78:81], v[78:81], v[228:231], v[82:85]
	s_waitcnt vmcnt(14)
	v_mfma_f32_16x16x32_f16 v[58:61], v[122:125], v[180:183], v[58:61]
	v_mfma_f32_16x16x32_f16 v[82:85], v[122:125], v[220:223], v[86:89]
	v_mfma_f32_16x16x32_f16 v[86:89], v[122:125], v[224:227], v[94:97]
	v_mfma_f32_16x16x32_f16 v[70:73], v[122:125], v[228:231], v[70:73]
	s_waitcnt vmcnt(13)
	v_mfma_f32_16x16x32_f16 v[54:57], v[156:159], v[180:183], v[54:57]
	v_mfma_f32_16x16x32_f16 v[74:77], v[156:159], v[220:223], v[74:77]
	v_mfma_f32_16x16x32_f16 v[90:93], v[156:159], v[224:227], v[90:93]
	v_mfma_f32_16x16x32_f16 v[62:65], v[156:159], v[228:231], v[62:65]
	s_waitcnt vmcnt(12)
	v_mfma_f32_16x16x32_f16 v[38:41], v[160:163], v[180:183], v[38:41]
	buffer_load_dwordx4 v[94:97], v147, s[16:19], s8 offen
	buffer_load_dwordx4 v[122:125], v148, s[16:19], s8 offen
	buffer_load_dwordx4 v[156:159], v149, s[16:19], s8 offen
	buffer_load_dwordx4 v[180:183], v150, s[16:19], s8 offen
	v_mfma_f32_16x16x32_f16 v[42:45], v[160:163], v[220:223], v[42:45]
	v_mfma_f32_16x16x32_f16 v[46:49], v[160:163], v[224:227], v[46:49]
	v_mfma_f32_16x16x32_f16 v[34:37], v[160:163], v[228:231], v[34:37]
	v_add_u32_e32 v98, s73, v98
	ds_read_b128 v[160:163], v98
	ds_read_b128 v[220:223], v98 offset:16384
	ds_read_b128 v[224:227], v98 offset:32768
	ds_read_b128 v[228:231], v98 offset:49152
	s_add_i32 s8, s22, s42
	s_waitcnt vmcnt(15) lgkmcnt(7)
	v_mfma_f32_16x16x32_f16 v[164:167], v[66:69], v[188:191], v[164:167]
	s_waitcnt lgkmcnt(6)
	v_mfma_f32_16x16x32_f16 v[168:171], v[66:69], v[208:211], v[168:171]
	s_waitcnt lgkmcnt(5)
	v_mfma_f32_16x16x32_f16 v[172:175], v[66:69], v[212:215], v[172:175]
	s_waitcnt lgkmcnt(4)
	v_mfma_f32_16x16x32_f16 v[66:69], v[66:69], v[216:219], v[78:81]
	s_waitcnt vmcnt(14)
	v_mfma_f32_16x16x32_f16 v[58:61], v[192:195], v[188:191], v[58:61]
	v_mfma_f32_16x16x32_f16 v[78:81], v[192:195], v[208:211], v[82:85]
	v_mfma_f32_16x16x32_f16 v[82:85], v[192:195], v[212:215], v[86:89]
	v_mfma_f32_16x16x32_f16 v[70:73], v[192:195], v[216:219], v[70:73]
	s_waitcnt vmcnt(13)
	v_mfma_f32_16x16x32_f16 v[54:57], v[196:199], v[188:191], v[54:57]
	v_mfma_f32_16x16x32_f16 v[74:77], v[196:199], v[208:211], v[74:77]
	v_mfma_f32_16x16x32_f16 v[86:89], v[196:199], v[212:215], v[90:93]
	v_mfma_f32_16x16x32_f16 v[62:65], v[196:199], v[216:219], v[62:65]
	s_waitcnt vmcnt(12)
	v_mfma_f32_16x16x32_f16 v[38:41], v[200:203], v[188:191], v[38:41]
	buffer_load_dwordx4 v[90:93], v147, s[16:19], s8 offen
	buffer_load_dwordx4 v[188:191], v148, s[16:19], s8 offen
	buffer_load_dwordx4 v[192:195], v149, s[16:19], s8 offen
	buffer_load_dwordx4 v[196:199], v150, s[16:19], s8 offen
	v_mfma_f32_16x16x32_f16 v[42:45], v[200:203], v[208:211], v[42:45]
	v_mfma_f32_16x16x32_f16 v[46:49], v[200:203], v[212:215], v[46:49]
	v_mfma_f32_16x16x32_f16 v[34:37], v[200:203], v[216:219], v[34:37]
	v_add_u32_e32 v99, s74, v99
	ds_read_b128 v[200:203], v99
	ds_read_b128 v[208:211], v99 offset:16384
	ds_read_b128 v[212:215], v99 offset:32768
	ds_read_b128 v[216:219], v99 offset:49152
	s_add_i32 s8, s22, s43
	s_waitcnt vmcnt(15) lgkmcnt(7)
	v_mfma_f32_16x16x32_f16 v[164:167], v[50:53], v[160:163], v[164:167]
	s_waitcnt lgkmcnt(6)
	v_mfma_f32_16x16x32_f16 v[168:171], v[50:53], v[220:223], v[168:171]
	s_waitcnt lgkmcnt(5)
	v_mfma_f32_16x16x32_f16 v[172:175], v[50:53], v[224:227], v[172:175]
	s_waitcnt lgkmcnt(4)
	v_mfma_f32_16x16x32_f16 v[50:53], v[50:53], v[228:231], v[66:69]
	s_waitcnt vmcnt(14)
	v_mfma_f32_16x16x32_f16 v[58:61], v[140:143], v[160:163], v[58:61]
	v_mfma_f32_16x16x32_f16 v[66:69], v[140:143], v[220:223], v[78:81]
	v_mfma_f32_16x16x32_f16 v[78:81], v[140:143], v[224:227], v[82:85]
	v_mfma_f32_16x16x32_f16 v[70:73], v[140:143], v[228:231], v[70:73]
	s_waitcnt vmcnt(13)
	v_mfma_f32_16x16x32_f16 v[54:57], v[152:155], v[160:163], v[54:57]
	v_mfma_f32_16x16x32_f16 v[74:77], v[152:155], v[220:223], v[74:77]
	v_mfma_f32_16x16x32_f16 v[82:85], v[152:155], v[224:227], v[86:89]
	v_mfma_f32_16x16x32_f16 v[62:65], v[152:155], v[228:231], v[62:65]
	s_waitcnt vmcnt(12)
	v_mfma_f32_16x16x32_f16 v[38:41], v[176:179], v[160:163], v[38:41]
	buffer_load_dwordx4 v[86:89], v147, s[16:19], s8 offen
	buffer_load_dwordx4 v[140:143], v148, s[16:19], s8 offen
	buffer_load_dwordx4 v[152:155], v149, s[16:19], s8 offen
	buffer_load_dwordx4 v[160:163], v150, s[16:19], s8 offen
	v_mfma_f32_16x16x32_f16 v[42:45], v[176:179], v[220:223], v[42:45]
	v_mfma_f32_16x16x32_f16 v[46:49], v[176:179], v[224:227], v[46:49]
	v_mfma_f32_16x16x32_f16 v[34:37], v[176:179], v[228:231], v[34:37]
	v_add_u32_e32 v100, s75, v100
	ds_read_b128 v[176:179], v100
	ds_read_b128 v[220:223], v100 offset:16384
	ds_read_b128 v[224:227], v100 offset:32768
	ds_read_b128 v[228:231], v100 offset:49152
	s_add_i32 s8, s22, s44
	s_waitcnt vmcnt(15) lgkmcnt(7)
	v_mfma_f32_16x16x32_f16 v[164:167], v[126:129], v[200:203], v[164:167]
	s_waitcnt lgkmcnt(6)
	v_mfma_f32_16x16x32_f16 v[168:171], v[126:129], v[208:211], v[168:171]
	s_waitcnt lgkmcnt(5)
	v_mfma_f32_16x16x32_f16 v[172:175], v[126:129], v[212:215], v[172:175]
	s_waitcnt lgkmcnt(4)
	v_mfma_f32_16x16x32_f16 v[50:53], v[126:129], v[216:219], v[50:53]
	s_waitcnt vmcnt(14)
	v_mfma_f32_16x16x32_f16 v[58:61], v[136:139], v[200:203], v[58:61]
	v_mfma_f32_16x16x32_f16 v[66:69], v[136:139], v[208:211], v[66:69]
	v_mfma_f32_16x16x32_f16 v[78:81], v[136:139], v[212:215], v[78:81]
	v_mfma_f32_16x16x32_f16 v[70:73], v[136:139], v[216:219], v[70:73]
	s_waitcnt vmcnt(13)
	v_mfma_f32_16x16x32_f16 v[54:57], v[184:187], v[200:203], v[54:57]
	v_mfma_f32_16x16x32_f16 v[74:77], v[184:187], v[208:211], v[74:77]
	v_mfma_f32_16x16x32_f16 v[82:85], v[184:187], v[212:215], v[82:85]
	v_mfma_f32_16x16x32_f16 v[62:65], v[184:187], v[216:219], v[62:65]
	s_waitcnt vmcnt(12)
	v_mfma_f32_16x16x32_f16 v[38:41], v[204:207], v[200:203], v[38:41]
	buffer_load_dwordx4 v[126:129], v147, s[16:19], s8 offen
	buffer_load_dwordx4 v[136:139], v148, s[16:19], s8 offen
	buffer_load_dwordx4 v[184:187], v149, s[16:19], s8 offen
	buffer_load_dwordx4 v[200:203], v150, s[16:19], s8 offen
	v_mfma_f32_16x16x32_f16 v[42:45], v[204:207], v[208:211], v[42:45]
	v_mfma_f32_16x16x32_f16 v[46:49], v[204:207], v[212:215], v[46:49]
	v_mfma_f32_16x16x32_f16 v[34:37], v[204:207], v[216:219], v[34:37]
	v_add_u32_e32 v111, s76, v111
	ds_read_b128 v[204:207], v111
	ds_read_b128 v[208:211], v111 offset:16384
	ds_read_b128 v[212:215], v111 offset:32768
	ds_read_b128 v[216:219], v111 offset:49152
	s_add_i32 s8, s22, s45
	s_waitcnt vmcnt(15) lgkmcnt(7)
	v_mfma_f32_16x16x32_f16 v[164:167], v[94:97], v[176:179], v[164:167]
	s_waitcnt lgkmcnt(6)
	v_mfma_f32_16x16x32_f16 v[168:171], v[94:97], v[220:223], v[168:171]
	s_waitcnt vmcnt(14)
	v_mfma_f32_16x16x32_f16 v[58:61], v[122:125], v[176:179], v[58:61]
	v_mfma_f32_16x16x32_f16 v[66:69], v[122:125], v[220:223], v[66:69]
	s_waitcnt lgkmcnt(5)
	v_mfma_f32_16x16x32_f16 v[78:81], v[122:125], v[224:227], v[78:81]
	s_waitcnt lgkmcnt(4)
	v_mfma_f32_16x16x32_f16 v[70:73], v[122:125], v[228:231], v[70:73]
	s_waitcnt vmcnt(13)
	v_mfma_f32_16x16x32_f16 v[54:57], v[156:159], v[176:179], v[54:57]
	v_mfma_f32_16x16x32_f16 v[74:77], v[156:159], v[220:223], v[74:77]
	v_mfma_f32_16x16x32_f16 v[82:85], v[156:159], v[224:227], v[82:85]
	v_mfma_f32_16x16x32_f16 v[62:65], v[156:159], v[228:231], v[62:65]
	s_waitcnt vmcnt(12)
	v_mfma_f32_16x16x32_f16 v[38:41], v[180:183], v[176:179], v[38:41]
	v_mfma_f32_16x16x32_f16 v[42:45], v[180:183], v[220:223], v[42:45]
	buffer_load_dwordx4 v[122:125], v147, s[16:19], s8 offen
	buffer_load_dwordx4 v[156:159], v148, s[16:19], s8 offen
	buffer_load_dwordx4 v[176:179], v149, s[16:19], s8 offen
	buffer_load_dwordx4 v[220:223], v150, s[16:19], s8 offen
	v_mfma_f32_16x16x32_f16 v[50:53], v[94:97], v[228:231], v[50:53]
	v_mfma_f32_16x16x32_f16 v[46:49], v[180:183], v[224:227], v[46:49]
	v_mfma_f32_16x16x32_f16 v[34:37], v[180:183], v[228:231], v[34:37]
	v_mfma_f32_16x16x32_f16 v[172:175], v[94:97], v[224:227], v[172:175]
	v_add_u32_e32 v98, s77, v98
	ds_read_b128 v[94:97], v98
	ds_read_b128 v[180:183], v98 offset:16384
	ds_read_b128 v[224:227], v98 offset:32768
	ds_read_b128 v[228:231], v98 offset:49152
	s_add_i32 s8, s22, s46
	s_waitcnt vmcnt(15) lgkmcnt(7)
	v_mfma_f32_16x16x32_f16 v[164:167], v[90:93], v[204:207], v[164:167]
	s_waitcnt lgkmcnt(6)
	v_mfma_f32_16x16x32_f16 v[168:171], v[90:93], v[208:211], v[168:171]
	s_waitcnt lgkmcnt(5)
	v_mfma_f32_16x16x32_f16 v[172:175], v[90:93], v[212:215], v[172:175]
	s_waitcnt lgkmcnt(4)
	v_mfma_f32_16x16x32_f16 v[90:93], v[90:93], v[216:219], v[50:53]
	s_waitcnt vmcnt(14)
	v_mfma_f32_16x16x32_f16 v[232:235], v[188:191], v[204:207], v[58:61]
	v_mfma_f32_16x16x32_f16 v[66:69], v[188:191], v[208:211], v[66:69]
	v_mfma_f32_16x16x32_f16 v[78:81], v[188:191], v[212:215], v[78:81]
	v_mfma_f32_16x16x32_f16 v[70:73], v[188:191], v[216:219], v[70:73]
	s_waitcnt vmcnt(13)
	v_mfma_f32_16x16x32_f16 v[188:191], v[192:195], v[204:207], v[54:57]
	v_mfma_f32_16x16x32_f16 v[74:77], v[192:195], v[208:211], v[74:77]
	v_mfma_f32_16x16x32_f16 v[82:85], v[192:195], v[212:215], v[82:85]
	v_mfma_f32_16x16x32_f16 v[62:65], v[192:195], v[216:219], v[62:65]
	s_waitcnt vmcnt(12)
	v_mfma_f32_16x16x32_f16 v[192:195], v[196:199], v[204:207], v[38:41]
	buffer_load_dwordx4 v[58:61], v147, s[16:19], s8 offen
	buffer_load_dwordx4 v[54:57], v148, s[16:19], s8 offen
	buffer_load_dwordx4 v[50:53], v149, s[16:19], s8 offen
	buffer_load_dwordx4 v[38:41], v150, s[16:19], s8 offen
	v_mfma_f32_16x16x32_f16 v[42:45], v[196:199], v[208:211], v[42:45]
	v_mfma_f32_16x16x32_f16 v[46:49], v[196:199], v[212:215], v[46:49]
	v_mfma_f32_16x16x32_f16 v[196:199], v[196:199], v[216:219], v[34:37]
	v_add_u32_e32 v99, s78, v99
	ds_read_b128 v[204:207], v99
	ds_read_b128 v[208:211], v99 offset:16384
	ds_read_b128 v[212:215], v99 offset:32768
	ds_read_b128 v[216:219], v99 offset:49152
	s_add_i32 s8, s22, s47
	s_waitcnt vmcnt(15) lgkmcnt(7)
	v_mfma_f32_16x16x32_f16 v[164:167], v[86:89], v[94:97], v[164:167]
	s_waitcnt lgkmcnt(6)
	v_mfma_f32_16x16x32_f16 v[168:171], v[86:89], v[180:183], v[168:171]
	s_waitcnt lgkmcnt(5)
	v_mfma_f32_16x16x32_f16 v[172:175], v[86:89], v[224:227], v[172:175]
	s_waitcnt lgkmcnt(4)
	v_mfma_f32_16x16x32_f16 v[86:89], v[86:89], v[228:231], v[90:93]
	s_waitcnt vmcnt(14)
	v_mfma_f32_16x16x32_f16 v[232:235], v[140:143], v[94:97], v[232:235]
	v_mfma_f32_16x16x32_f16 v[66:69], v[140:143], v[180:183], v[66:69]
	v_mfma_f32_16x16x32_f16 v[236:239], v[140:143], v[224:227], v[78:81]
	v_mfma_f32_16x16x32_f16 v[70:73], v[140:143], v[228:231], v[70:73]
	s_waitcnt vmcnt(13)
	v_mfma_f32_16x16x32_f16 v[140:143], v[152:155], v[94:97], v[188:191]
	v_mfma_f32_16x16x32_f16 v[74:77], v[152:155], v[180:183], v[74:77]
	v_mfma_f32_16x16x32_f16 v[82:85], v[152:155], v[224:227], v[82:85]
	v_mfma_f32_16x16x32_f16 v[62:65], v[152:155], v[228:231], v[62:65]
	s_waitcnt vmcnt(12)
	v_mfma_f32_16x16x32_f16 v[152:155], v[160:163], v[94:97], v[192:195]
	buffer_load_dwordx4 v[94:97], v147, s[16:19], s8 offen
	buffer_load_dwordx4 v[90:93], v148, s[16:19], s8 offen
	buffer_load_dwordx4 v[78:81], v149, s[16:19], s8 offen
	buffer_load_dwordx4 v[34:37], v150, s[16:19], s8 offen
	v_mfma_f32_16x16x32_f16 v[42:45], v[160:163], v[180:183], v[42:45]
	v_mfma_f32_16x16x32_f16 v[46:49], v[160:163], v[224:227], v[46:49]
	v_mfma_f32_16x16x32_f16 v[160:163], v[160:163], v[228:231], v[196:199]
	v_add_u32_e32 v100, s79, v100
	ds_read_b128 v[180:183], v100
	ds_read_b128 v[188:191], v100 offset:16384
	ds_read_b128 v[192:195], v100 offset:32768
	ds_read_b128 v[196:199], v100 offset:49152
	s_add_i32 s8, s22, s48
	s_waitcnt vmcnt(15) lgkmcnt(7)
	v_mfma_f32_16x16x32_f16 v[164:167], v[126:129], v[204:207], v[164:167]
	s_waitcnt lgkmcnt(6)
	v_mfma_f32_16x16x32_f16 v[168:171], v[126:129], v[208:211], v[168:171]
	s_waitcnt lgkmcnt(5)
	v_mfma_f32_16x16x32_f16 v[172:175], v[126:129], v[212:215], v[172:175]
	s_waitcnt lgkmcnt(4)
	v_mfma_f32_16x16x32_f16 v[86:89], v[126:129], v[216:219], v[86:89]
	s_waitcnt vmcnt(14)
	v_mfma_f32_16x16x32_f16 v[126:129], v[136:139], v[204:207], v[232:235]
	v_mfma_f32_16x16x32_f16 v[66:69], v[136:139], v[208:211], v[66:69]
	v_mfma_f32_16x16x32_f16 v[224:227], v[136:139], v[212:215], v[236:239]
	v_mfma_f32_16x16x32_f16 v[136:139], v[136:139], v[216:219], v[70:73]
	s_waitcnt vmcnt(13)
	v_mfma_f32_16x16x32_f16 v[140:143], v[184:187], v[204:207], v[140:143]
	v_mfma_f32_16x16x32_f16 v[74:77], v[184:187], v[208:211], v[74:77]
	v_mfma_f32_16x16x32_f16 v[228:231], v[184:187], v[212:215], v[82:85]
	v_mfma_f32_16x16x32_f16 v[184:187], v[184:187], v[216:219], v[62:65]
	s_waitcnt vmcnt(12)
	v_mfma_f32_16x16x32_f16 v[152:155], v[200:203], v[204:207], v[152:155]
	v_mfma_f32_16x16x32_f16 v[204:207], v[200:203], v[208:211], v[42:45]
	buffer_load_dwordx4 v[82:85], v147, s[16:19], s8 offen
	buffer_load_dwordx4 v[70:73], v148, s[16:19], s8 offen
	buffer_load_dwordx4 v[62:65], v149, s[16:19], s8 offen
	buffer_load_dwordx4 v[42:45], v150, s[16:19], s8 offen
	v_mfma_f32_16x16x32_f16 v[46:49], v[200:203], v[212:215], v[46:49]
	v_mfma_f32_16x16x32_f16 v[160:163], v[200:203], v[216:219], v[160:163]
	v_add_u32_e32 v0, 0x1ac00, v104
	ds_read_b128 v[240:243], v0
	ds_read_b128 v[244:247], v0 offset:16
	s_waitcnt vmcnt(12) lgkmcnt(5)
	v_mfma_f32_16x16x32_f16 v[164:167], v[122:125], v[180:183], v[164:167]
	v_mfma_f32_16x16x32_f16 v[126:129], v[156:159], v[180:183], v[126:129]
	v_mfma_f32_16x16x32_f16 v[140:143], v[176:179], v[180:183], v[140:143]
	v_mfma_f32_16x16x32_f16 v[152:155], v[220:223], v[180:183], v[152:155]
	s_waitcnt lgkmcnt(4)
	v_mfma_f32_16x16x32_f16 v[168:171], v[122:125], v[188:191], v[168:171]
	v_mfma_f32_16x16x32_f16 v[208:211], v[156:159], v[188:191], v[66:69]
	v_mfma_f32_16x16x32_f16 v[212:215], v[176:179], v[188:191], v[74:77]
	v_mfma_f32_16x16x32_f16 v[204:207], v[220:223], v[188:191], v[204:207]
	s_waitcnt lgkmcnt(3)
	v_mfma_f32_16x16x32_f16 v[172:175], v[122:125], v[192:195], v[172:175]
	v_cvt_pk_f16_f32 v232, v164, v165
	v_cvt_pk_f16_f32 v233, v166, v167
	v_pk_max_f16 v232, v232, 0
	v_pk_max_f16 v233, v233, 0
	v_mfma_f32_16x16x32_f16 v[224:227], v[156:159], v[192:195], v[224:227]
	v_cvt_pk_f16_f32 v234, v126, v127
	v_cvt_pk_f16_f32 v235, v128, v129
	v_pk_max_f16 v234, v234, 0
	v_pk_max_f16 v235, v235, 0
	v_mfma_f32_16x16x32_f16 v[228:231], v[176:179], v[192:195], v[228:231]
	v_cvt_pk_f16_f32 v236, v140, v141
	v_cvt_pk_f16_f32 v237, v142, v143
	v_pk_max_f16 v236, v236, 0
	v_pk_max_f16 v237, v237, 0
	v_mfma_f32_16x16x32_f16 v[216:219], v[220:223], v[192:195], v[46:49]
	v_cvt_pk_f16_f32 v238, v152, v153
	v_cvt_pk_f16_f32 v239, v154, v155
	v_pk_max_f16 v238, v238, 0
	v_pk_max_f16 v239, v239, 0
	s_waitcnt lgkmcnt(2)
	v_mfma_f32_16x16x32_f16 v[200:203], v[122:125], v[196:199], v[86:89]
	v_cvt_pk_f16_f32 v180, v168, v169
	v_cvt_pk_f16_f32 v181, v170, v171
	v_pk_max_f16 v180, v180, 0
	v_pk_max_f16 v181, v181, 0
	s_add_i32 s8, s22, s49
	buffer_load_dwordx4 v[86:89], v147, s[16:19], s8 offen
	buffer_load_dwordx4 v[74:77], v148, s[16:19], s8 offen
	buffer_load_dwordx4 v[66:69], v149, s[16:19], s8 offen
	buffer_load_dwordx4 v[46:49], v150, s[16:19], s8 offen
	v_mfma_f32_16x16x32_f16 v[136:139], v[156:159], v[196:199], v[136:139]
	v_cvt_pk_f16_f32 v182, v208, v209
	v_cvt_pk_f16_f32 v183, v210, v211
	v_pk_max_f16 v182, v182, 0
	v_pk_max_f16 v183, v183, 0
	s_waitcnt lgkmcnt(1)
	v_mfma_f32_16x16x32_f16 v[252:255], v[240:243], v[232:235], 0
	v_cvt_pk_f16_f32 v232, v172, v173
	v_cvt_pk_f16_f32 v233, v174, v175
	v_pk_max_f16 v232, v232, 0
	v_pk_max_f16 v233, v233, 0
	v_mfma_f32_16x16x32_f16 v[184:187], v[176:179], v[196:199], v[184:187]
	v_cvt_pk_f16_f32 v188, v212, v213
	v_cvt_pk_f16_f32 v189, v214, v215
	v_pk_max_f16 v188, v188, 0
	v_pk_max_f16 v189, v189, 0
	s_waitcnt lgkmcnt(0)
	v_mfma_f32_16x16x32_f16 v[252:255], v[244:247], v[236:239], v[252:255]
	v_cvt_pk_f16_f32 v234, v224, v225
	v_cvt_pk_f16_f32 v235, v226, v227
	v_pk_max_f16 v234, v234, 0
	v_pk_max_f16 v235, v235, 0
	v_mfma_f32_16x16x32_f16 v[160:163], v[220:223], v[196:199], v[160:163]
	v_cvt_pk_f16_f32 v190, v204, v205
	v_cvt_pk_f16_f32 v191, v206, v207
	v_pk_max_f16 v190, v190, 0
	v_pk_max_f16 v191, v191, 0
	v_mfma_f32_16x16x32_f16 v[192:195], v[240:243], v[180:183], 0
	v_cvt_pk_f16_f32 v236, v228, v229
	v_cvt_pk_f16_f32 v237, v230, v231
	v_pk_max_f16 v236, v236, 0
	v_pk_max_f16 v237, v237, 0
	v_mfma_f32_16x16x32_f16 v[192:195], v[244:247], v[188:191], v[192:195]
	v_cvt_pk_f16_f32 v238, v216, v217
	v_cvt_pk_f16_f32 v239, v218, v219
	v_pk_max_f16 v238, v238, 0
	v_pk_max_f16 v239, v239, 0
	v_cvt_pk_f16_f32 v180, v200, v201
	v_cvt_pk_f16_f32 v181, v202, v203
	v_pk_max_f16 v180, v180, 0
	v_pk_max_f16 v181, v181, 0
	v_mfma_f32_16x16x32_f16 v[196:199], v[240:243], v[232:235], 0
	v_cvt_pk_f16_f32 v182, v136, v137
	v_cvt_pk_f16_f32 v183, v138, v139
	v_pk_max_f16 v182, v182, 0
	v_pk_max_f16 v183, v183, 0
	v_mfma_f32_16x16x32_f16 v[196:199], v[244:247], v[236:239], v[196:199]
	v_cvt_pk_f16_f32 v188, v184, v185
	v_cvt_pk_f16_f32 v189, v186, v187
	v_pk_max_f16 v188, v188, 0
	v_pk_max_f16 v189, v189, 0
	v_cvt_pk_f16_f32 v190, v160, v161
	v_cvt_pk_f16_f32 v191, v162, v163
	v_pk_max_f16 v190, v190, 0
	v_pk_max_f16 v191, v191, 0
	v_mfma_f32_16x16x32_f16 v[122:125], v[240:243], v[180:183], 0
	s_nop 0
	v_mfma_f32_16x16x32_f16 v[122:125], v[244:247], v[188:191], v[122:125]
	v_add_u32_e32 v145, 0x12c00, v105
	ds_read_b128 v[240:243], v145 offset:2048
	ds_read_b128 v[244:247], v145 offset:2064
	ds_read_b128 v[248:251], v145 offset:2080
	s_load_dword s30, s[12:13], 0x0
	v_cndmask_b32_e64 v0, v252, v192, s[2:3]
	ds_read_b128 v[252:255], v145 offset:2096
	ds_read_u16 v102, v114
	ds_read_u16 v103, v114 offset:512
	ds_read_u16 v115, v114 offset:1024
	ds_read_u16 v116, v114 offset:1536
	v_cndmask_b32_e64 v0, v0, v196, s[0:1]
	s_waitcnt vmcnt(16)
	v_cndmask_b32_e64 v1, v30, v134, s[0:1]
	v_bfi_b32 v30, s10, v1, v30
	v_perm_b32 v1, v22, v134, s24
	v_cndmask_b32_e64 v22, v22, v1, s[0:1]
	v_bfi_b32 v1, s10, v135, v18
	v_perm_b32 v121, v10, v135, s24
	v_cndmask_b32_e64 v18, v18, v1, s[0:1]
	v_cndmask_b32_e64 v10, v10, v121, s[0:1]
	v_cndmask_b32_e64 v0, v0, v122, s[26:27]
	ds_write_b32 v112, v0
	s_add_i32 s22, s22, 0x80000
	s_add_i32 s11, s11, 1
	s_add_u32 s12, s12, 4
	s_addc_u32 s13, s13, 0
	v_add_u32_e32 v104, 0x400, v104
	v_add_u32_e32 v105, 0x800, v105
	v_add_u32_e32 v114, 2, v114
	s_cmp_eq_u32 s22, 0x898000
	s_waitcnt lgkmcnt(0)
	s_barrier
	ds_read_b128 v[232:235], v113
	ds_read_b128 v[236:239], v113 offset:1024
	s_waitcnt lgkmcnt(0)
	v_add_f32_e32 v0, v232, v233
	v_add_f32_e32 v1, v234, v235
	v_add_f32_e32 v121, v236, v237
	v_add_f32_e32 v144, v238, v239
	v_add_f32_e32 v0, v0, v1
	v_add_f32_e32 v121, v121, v144
	v_add_f32_e32 v0, v0, v121
	v_add_f32_e32 v0, s30, v0
	ds_write_b32 v106, v0
	v_cvt_f16_f32_e32 v1, v0
	v_cvt_f16_f32_e32 v121, v0
	s_nop 1
	v_permlane16_swap_b32_e32 v1, v121
	v_mov_b32_e32 v144, v1
	v_mov_b32_e32 v145, v121
	s_nop 1
	v_permlane32_swap_b32_e32 v1, v144
	v_permlane32_swap_b32_e32 v121, v145
	v_add_u32_e32 v106, 4, v106
	s_cbranch_scc0 .LBB1_4
